# MoE K-loops: end-of-K-tile drain split into counted waits (weights first, convert + issue next weight loads, then the LDS-DMA A loads before the barrier)
# speedup vs baseline: 1.0143x; 1.0064x over previous
.LBB0_730:
	s_add_i32 s38, s4, 2
	s_cmp_eq_u32 s34, 28
	s_cselect_b64 s[4:5], -1, 0
	s_and_b64 s[34:35], s[4:5], exec
	s_cselect_b32 s38, 0, s38
	s_cselect_b32 s34, s23, s37
	s_cselect_b32 s35, s22, s36
	s_cselect_b32 s66, s21, s25
	s_cselect_b32 s67, s20, s24
	s_cmp_lg_u64 s[2:3], 0
	s_cbranch_scc1 .Lw2_guE
	s_waitcnt vmcnt(4)
	s_branch .Lwd_guE
.Lw2_guE:
	s_waitcnt vmcnt(2)
.Lwd_guE:
	v_cvt_pk_bf16_f32 v2, v2, v3
	v_cvt_pk_bf16_f32 v3, v4, v5
	s_ashr_i32 s39, s38, 31
	ds_write_b64 v199, v[2:3]
	v_cvt_pk_bf16_f32 v2, v6, v7
	v_cvt_pk_bf16_f32 v3, v8, v9
	s_lshl_b64 s[40:41], s[38:39], 18
	ds_write_b64 v200, v[2:3]
	v_cvt_pk_bf16_f32 v2, v10, v11
	v_cvt_pk_bf16_f32 v3, v12, v13
	s_add_u32 s68, s67, s40
	ds_write_b64 v201, v[2:3]
	v_cvt_pk_bf16_f32 v2, v14, v15
	v_cvt_pk_bf16_f32 v3, v16, v17
	s_addc_u32 s69, s66, s41
	ds_write_b64 v202, v[2:3]
	v_cvt_pk_bf16_f32 v2, v18, v19
	v_cvt_pk_bf16_f32 v3, v20, v21
	s_add_u32 s40, s35, s40
	ds_write_b64 v203, v[2:3]
	v_cvt_pk_bf16_f32 v2, v22, v23
	v_cvt_pk_bf16_f32 v3, v24, v25
	s_addc_u32 s41, s34, s41
	ds_write_b64 v204, v[2:3]
	v_cvt_pk_bf16_f32 v2, v26, v27
	v_cvt_pk_bf16_f32 v3, v28, v29
	s_add_u32 s70, s68, 0x2000
	ds_write_b64 v205, v[2:3]
	v_cvt_pk_bf16_f32 v2, v34, v35
	v_cvt_pk_bf16_f32 v3, v36, v37
	ds_write_b64 v206, v[2:3]
	s_addc_u32 s71, s69, 0
	global_load_dwordx4 v[34:37], v189, s[68:69]
	s_add_u32 s72, s40, 0x2000
	global_load_dwordx4 v[22:25], v189, s[40:41]
	s_addc_u32 s73, s41, 0
	global_load_dwordx4 v[26:29], v189, s[70:71]
	s_add_u32 s70, s68, 0x4000
	s_addc_u32 s71, s69, 0
	global_load_dwordx4 v[14:17], v189, s[72:73]
	s_add_u32 s72, s40, 0x4000
	s_addc_u32 s73, s41, 0
	s_add_u32 s68, s68, 0x6000
	global_load_dwordx4 v[18:21], v189, s[70:71]
	s_addc_u32 s69, s69, 0
	global_load_dwordx4 v[6:9], v189, s[72:73]
	s_add_u32 s40, s40, 0x6000
	s_addc_u32 s41, s41, 0
	global_load_dwordx4 v[10:13], v189, s[68:69]
	global_load_dwordx4 v[2:5], v189, s[40:41]
	s_lshl_b64 s[40:41], s[38:39], 7
	s_add_u32 s40, s8, s40
	s_mov_b32 m0, s51
	s_waitcnt vmcnt(8)
	s_waitcnt lgkmcnt(0)
	s_barrier
	s_addc_u32 s41, s9, s41
	v_cndmask_b32_e64 v164, v178, v209, s[4:5]
	v_cndmask_b32_e64 v163, v180, v210, s[4:5]
	global_load_lds_dwordx4 v164, s[40:41]
	s_mov_b32 m0, s60
	v_cndmask_b32_e64 v162, v213, v208, s[4:5]
	global_load_lds_dwordx4 v163, s[40:41]
	v_cmp_ne_u32_e32 vcc, 0, v162
	s_mov_b64 s[96:97], vcc
	s_cbranch_vccnz .LBB0_732
	v_cndmask_b32_e64 v163, v182, v211, s[4:5]
	s_add_i32 m0, s51, 0x4000
	v_cndmask_b32_e64 v162, v184, v212, s[4:5]
	global_load_lds_dwordx4 v163, s[40:41]
	s_add_i32 m0, s51, 0x6000
	s_nop 0
	global_load_lds_dwordx4 v162, s[40:41]

.LBB0_736:
	s_lshl_b64 s[2:3], s[38:39], 18
	s_add_u32 s4, s2, 0x40000
	s_addc_u32 s5, s3, 0
	s_add_u32 s2, s67, s4
	s_addc_u32 s3, s66, s5
	s_cmp_lg_u64 s[96:97], 0
	s_cbranch_scc1 .Lw2_guO
	s_waitcnt vmcnt(4)
	s_branch .Lwd_guO

.Lwd_guO:
	v_cvt_pk_bf16_f32 v34, v34, v35
	v_cvt_pk_bf16_f32 v35, v36, v37
	ds_write_b64 v194, v[34:35]
	v_cvt_pk_bf16_f32 v22, v22, v23
	v_cvt_pk_bf16_f32 v23, v24, v25
	s_add_u32 s4, s35, s4
	ds_write_b64 v194, v[22:23] offset:16384
	v_cvt_pk_bf16_f32 v22, v26, v27
	v_cvt_pk_bf16_f32 v23, v28, v29
	ds_write_b64 v195, v[22:23]
	v_cvt_pk_bf16_f32 v14, v14, v15
	v_cvt_pk_bf16_f32 v15, v16, v17
	s_addc_u32 s5, s34, s5
	ds_write_b64 v195, v[14:15] offset:16384
	v_cvt_pk_bf16_f32 v14, v18, v19
	v_cvt_pk_bf16_f32 v15, v20, v21
	ds_write_b64 v196, v[14:15]
	v_cvt_pk_bf16_f32 v6, v6, v7
	v_cvt_pk_bf16_f32 v7, v8, v9
	s_add_u32 s34, s2, 0x2000
	ds_write_b64 v196, v[6:7] offset:16384
	v_cvt_pk_bf16_f32 v6, v10, v11
	v_cvt_pk_bf16_f32 v7, v12, v13
	ds_write_b64 v197, v[6:7]
	v_cvt_pk_bf16_f32 v2, v2, v3
	v_cvt_pk_bf16_f32 v3, v4, v5
	ds_write_b64 v197, v[2:3] offset:16384
	s_addc_u32 s35, s3, 0
	global_load_dwordx4 v[2:5], v189, s[2:3]
	s_add_u32 s38, s4, 0x2000
	global_load_dwordx4 v[6:9], v189, s[4:5]
	s_addc_u32 s39, s5, 0
	global_load_dwordx4 v[10:13], v189, s[34:35]
	s_add_u32 s34, s2, 0x4000
	s_addc_u32 s35, s3, 0
	global_load_dwordx4 v[14:17], v189, s[38:39]
	s_add_u32 s38, s4, 0x4000
	s_addc_u32 s39, s5, 0
	global_load_dwordx4 v[18:21], v189, s[34:35]
	s_add_u32 s2, s2, 0x6000
	global_load_dwordx4 v[22:25], v189, s[38:39]
	s_addc_u32 s3, s3, 0
	s_add_u32 s4, s4, 0x6000
	global_load_dwordx4 v[26:29], v189, s[2:3]
	s_addc_u32 s5, s5, 0
	global_load_dwordx4 v[34:37], v189, s[4:5]
	s_waitcnt vmcnt(8)
	s_waitcnt lgkmcnt(0)
	s_barrier
	s_cmp_gt_u32 s17, 29
	s_cbranch_scc1 .LBB0_738
	s_mov_b32 s34, s17
	s_branch .LBB0_724

.LBB0_862:
	s_add_i32 s48, s48, 2
	s_cmp_eq_u32 s35, 12
	s_cselect_b32 s48, 0, s48
	s_cselect_b32 s77, s41, s23
	s_cselect_b32 s82, s40, s22
	s_cselect_b32 s35, s39, s47
	s_cselect_b32 s37, s38, s46
	s_cselect_b32 s43, s27, s45
	s_cselect_b32 s74, s26, s44
	s_cselect_b64 vcc, -1, 0
	s_cmp_lg_u64 s[2:3], 0
	s_cbranch_scc1 .Lw2_dnE
	s_waitcnt vmcnt(4)
	s_branch .Lwd_dnE

.Lwd_dnE:
	v_cvt_pk_bf16_f32 v2, v64, v65
	v_cvt_pk_bf16_f32 v3, v66, v67
	s_ashr_i32 s49, s48, 31
	ds_write_b64 v199, v[2:3]
	v_cvt_pk_bf16_f32 v2, v60, v61
	v_cvt_pk_bf16_f32 v3, v62, v63
	s_lshl_b64 s[50:51], s[48:49], 19
	ds_write_b64 v200, v[2:3]
	v_cvt_pk_bf16_f32 v2, v76, v77
	v_cvt_pk_bf16_f32 v3, v78, v79
	s_add_u32 s72, s74, s50
	ds_write_b64 v201, v[2:3]
	v_cvt_pk_bf16_f32 v2, v72, v73
	v_cvt_pk_bf16_f32 v3, v74, v75
	s_addc_u32 s73, s43, s51
	ds_write_b64 v202, v[2:3]
	v_cvt_pk_bf16_f32 v2, v88, v89
	v_cvt_pk_bf16_f32 v3, v90, v91
	s_add_u32 s50, s37, s50
	ds_write_b64 v203, v[2:3]
	v_cvt_pk_bf16_f32 v2, v84, v85
	v_cvt_pk_bf16_f32 v3, v86, v87
	s_addc_u32 s51, s35, s51
	ds_write_b64 v204, v[2:3]
	v_cvt_pk_bf16_f32 v2, v96, v97
	v_cvt_pk_bf16_f32 v3, v98, v99
	s_add_u32 s78, s72, 0x4000
	ds_write_b64 v205, v[2:3]
	v_cvt_pk_bf16_f32 v2, v92, v93
	v_cvt_pk_bf16_f32 v3, v94, v95
	ds_write_b64 v206, v[2:3]
	s_addc_u32 s79, s73, 0
	global_load_dwordx4 v[96:99], v189, s[72:73]
	s_add_u32 s80, s50, 0x4000
	global_load_dwordx4 v[88:91], v189, s[50:51]
	s_addc_u32 s81, s51, 0
	global_load_dwordx4 v[92:95], v189, s[78:79]
	s_add_u32 s78, s72, 0x8000
	s_addc_u32 s79, s73, 0
	global_load_dwordx4 v[76:79], v189, s[80:81]
	s_add_u32 s80, s50, 0x8000
	s_addc_u32 s81, s51, 0
	s_add_u32 s72, s72, 0xc000
	global_load_dwordx4 v[84:87], v189, s[78:79]
	s_addc_u32 s73, s73, 0
	global_load_dwordx4 v[64:67], v189, s[80:81]
	s_add_u32 s50, s50, 0xc000
	s_addc_u32 s51, s51, 0
	global_load_dwordx4 v[72:75], v189, s[72:73]
	global_load_dwordx4 v[60:63], v189, s[50:51]
	s_lshl_b64 s[50:51], s[48:49], 7
	s_add_u32 s50, s82, s50
	s_addc_u32 s51, s77, s51
	s_mov_b32 m0, s21
	s_waitcnt vmcnt(8)
	s_waitcnt lgkmcnt(0)
	s_barrier
	v_lshl_add_u64 v[2:3], s[50:51], 0, v[180:181]
	global_load_lds_dwordx4 v[2:3], off
	v_lshl_add_u64 v[2:3], s[50:51], 0, v[182:183]
	s_mov_b32 m0, s67
	v_cndmask_b32_e32 v1, v209, v208, vcc
	global_load_lds_dwordx4 v[2:3], off
	v_cmp_ne_u32_e32 vcc, 0, v1
	s_mov_b64 s[96:97], vcc
	s_cbranch_vccnz .LBB0_864
	v_lshl_add_u64 v[164:165], s[50:51], 0, v[184:185]
	s_add_i32 m0, s21, 0x4000
	v_lshl_add_u64 v[2:3], s[50:51], 0, v[186:187]
	global_load_lds_dwordx4 v[164:165], off
	s_add_i32 m0, s21, 0x6000
	s_nop 0
	global_load_lds_dwordx4 v[2:3], off

.LBB0_868:
	s_lshl_b64 s[2:3], s[48:49], 19
	s_cmp_lg_u64 s[96:97], 0
	s_cbranch_scc1 .Lw2_dnO
	s_waitcnt vmcnt(4)
	s_branch .Lwd_dnO

.Lwd_dnO:
	s_add_u32 s48, s2, 0x80000
	v_cvt_pk_bf16_f32 v2, v96, v97
	v_cvt_pk_bf16_f32 v3, v98, v99
	ds_write_b64 v194, v[2:3]
	v_cvt_pk_bf16_f32 v2, v88, v89
	v_cvt_pk_bf16_f32 v3, v90, v91
	s_addc_u32 s49, s3, 0
	ds_write_b64 v194, v[2:3] offset:16384
	v_cvt_pk_bf16_f32 v2, v92, v93
	v_cvt_pk_bf16_f32 v3, v94, v95
	s_add_u32 s2, s74, s48
	ds_write_b64 v195, v[2:3]
	v_cvt_pk_bf16_f32 v2, v76, v77
	v_cvt_pk_bf16_f32 v3, v78, v79
	s_addc_u32 s3, s43, s49
	ds_write_b64 v195, v[2:3] offset:16384
	v_cvt_pk_bf16_f32 v2, v84, v85
	v_cvt_pk_bf16_f32 v3, v86, v87
	s_add_u32 s48, s37, s48
	ds_write_b64 v196, v[2:3]
	v_cvt_pk_bf16_f32 v2, v64, v65
	v_cvt_pk_bf16_f32 v3, v66, v67
	s_addc_u32 s49, s35, s49
	ds_write_b64 v196, v[2:3] offset:16384
	v_cvt_pk_bf16_f32 v2, v72, v73
	v_cvt_pk_bf16_f32 v3, v74, v75
	s_add_u32 s50, s2, 0x4000
	ds_write_b64 v197, v[2:3]
	v_cvt_pk_bf16_f32 v2, v60, v61
	v_cvt_pk_bf16_f32 v3, v62, v63
	ds_write_b64 v197, v[2:3] offset:16384
	s_addc_u32 s51, s3, 0
	global_load_dwordx4 v[64:67], v189, s[2:3]
	s_add_u32 s72, s48, 0x4000
	global_load_dwordx4 v[60:63], v189, s[48:49]
	s_addc_u32 s73, s49, 0
	global_load_dwordx4 v[76:79], v189, s[50:51]
	s_add_u32 s50, s2, 0x8000
	s_addc_u32 s51, s3, 0
	global_load_dwordx4 v[72:75], v189, s[72:73]
	s_add_u32 s72, s48, 0x8000
	s_addc_u32 s73, s49, 0
	global_load_dwordx4 v[88:91], v189, s[50:51]
	s_add_u32 s2, s2, 0xc000
	global_load_dwordx4 v[84:87], v189, s[72:73]
	s_addc_u32 s3, s3, 0
	s_add_u32 s48, s48, 0xc000
	global_load_dwordx4 v[96:99], v189, s[2:3]
	s_addc_u32 s49, s49, 0
	global_load_dwordx4 v[92:95], v189, s[48:49]
	s_waitcnt vmcnt(8)
	s_waitcnt lgkmcnt(0)
	s_barrier
	s_cmp_gt_u32 s34, 13
	s_cbranch_scc1 .LBB0_870
	s_mov_b32 s35, s34
	s_branch .LBB0_856
